# baseline (speedup 1.0000x reference)
_Z16sum_layer_kernelPKfS0_Pf:
	s_load_dwordx2 s[12:13], s[0:1], 0x8
	s_load_dwordx2 s[4:5], s[0:1], 0x0
	s_load_dwordx2 s[8:9], s[0:1], 0x10
	v_lshrrev_b32_e32 v42, 6, v0
	v_bfe_u32 v41, v0, 5, 1
	v_and_b32_e32 v40, 31, v0
	v_readfirstlane_b32 s23, v42
	v_and_b32_e32 v43, 7, v0
	v_bfe_u32 v44, v0, 3, 3
	s_lshl_b32 s3, s2, 12
	s_lshl_b32 s19, s2, 7
	s_lshl_b32 s23, s23, 12
	v_lshlrev_b32_e32 v1, 11, v41
	v_lshl_or_b32 v1, v40, 2, v1
	v_lshrrev_b32_e32 v46, 1, v44
	v_xor_b32_e32 v46, v43, v46
	v_lshlrev_b32_e32 v46, 4, v46
	v_lshl_add_u32 v35, v44, 16, v46
	v_lshl_add_u32 v35, v42, 21, v35
	v_add_u32_e32 v35, s19, v35
	v_xor_b32_e32 v86, 64, v35
	s_mov_b32 s20, 0x7fc00
	s_mov_b32 s21, 0xff800
	s_mov_b32 s22, 0x17f400
	s_mov_b32 s14, 0x200000
	s_mov_b32 s15, 0x20000
	v_and_b32_e32 v45, 63, v0
	v_lshlrev_b32_e32 v37, 4, v45
	s_add_u32 s54, s23, 0x4000
	s_mov_b32 s6, 0x800000
	s_mov_b32 s7, s15
	s_mov_b32 s10, s6
	s_mov_b32 s11, s15
	s_mov_b32 m0, s54
	s_waitcnt lgkmcnt(0)
	s_and_b32 s13, s13, 0xffff
	s_and_b32 s5, s5, 0xffff
	buffer_load_dwordx4 v37, s[12:15], s3 offen nt lds
	buffer_load_dwordx4 v37, s[12:15], s3 offen offset:1024 nt lds
	buffer_load_dwordx4 v37, s[12:15], s3 offen offset:2048 nt lds
	buffer_load_dwordx4 v37, s[12:15], s3 offen offset:3072 nt lds
	s_mov_b32 m0, s23
	s_nop 0
	buffer_load_dwordx4 v35, s[4:7], 0 offen nt lds
	buffer_load_dwordx4 v86, s[4:7], s20 offen offset:1024 nt lds
	buffer_load_dwordx4 v35, s[4:7], s21 offen offset:2048 nt lds
	buffer_load_dwordx4 v86, s[4:7], s22 offen offset:3072 nt lds
	v_and_b32_e32 v36, 30, v40
	v_lshlrev_b32_e32 v36, 2, v36
	v_and_b32_e32 v47, 1, v40
	v_lshl_add_u32 v36, v47, 16, v36
	v_lshl_add_u32 v36, v41, 18, v36
	v_lshl_add_u32 v36, v42, 21, v36
	v_add_u32_e32 v36, s19, v36
	v_bfe_u32 v47, v40, 1, 3
	v_lshlrev_b32_e32 v39, 2, v41
	v_xor_b32_e32 v39, v39, v47
	v_lshlrev_b32_e32 v39, 4, v39
	v_lshl_add_u32 v39, v40, 7, v39
	v_lshl_add_u32 v39, v42, 12, v39
	v_xor_b32_e32 v81, 16, v39
	v_xor_b32_e32 v82, 32, v39
	v_xor_b32_e32 v83, 48, v39
	v_cmp_gt_u32_e32 vcc, 32, v45
	v_mov_b32_e32 v34, 0xc1600000
	v_mov_b32_e32 v84, 0x3fb8aa3b
	v_mov_b32_e32 v85, 0x3f317218
	s_and_b32 s9, s9, 0xffff
	v_lshl_add_u32 v38, v42, 12, v1
	v_add_u32_e32 v38, 0x4000, v38
	v_add_u32_e32 v87, 0x400, v38
	s_waitcnt vmcnt(4)
	ds_read2_b32 v[18:19], v38 offset0:0 offset1:32
	ds_read2_b32 v[20:21], v38 offset0:64 offset1:96
	ds_read2_b32 v[22:23], v38 offset0:128 offset1:160
	ds_read2_b32 v[24:25], v38 offset0:192 offset1:224
	ds_read2_b32 v[26:27], v87 offset0:0 offset1:32
	ds_read2_b32 v[28:29], v87 offset0:64 offset1:96
	ds_read2_b32 v[30:31], v87 offset0:128 offset1:160
	ds_read2_b32 v[32:33], v87 offset0:192 offset1:224
	s_waitcnt lgkmcnt(0)
	v_max3_f32 v48, v18, v19, v20
	v_max3_f32 v50, v21, v22, v23
	v_max3_f32 v48, v48, v24, v25
	v_max3_f32 v50, v50, v26, v27
	v_max3_f32 v48, v48, v28, v29
	v_max3_f32 v50, v50, v30, v31
	v_max3_f32 v48, v48, v32, v33
	v_max_f32_e32 v48, v48, v50
	v_mov_b32_e32 v50, v48
	s_nop 1
	v_permlane32_swap_b32_e32 v48, v50
	v_max_f32_e32 v48, v48, v50
	v_fmamk_f32 v48, v48, 0x3fb8aa3b, v34
	v_pk_fma_f32 v[18:19], v[18:19], v[84:85], v[48:49] op_sel_hi:[1,0,0] neg_lo:[0,0,1] neg_hi:[0,0,1]
	v_exp_f32_e32 v18, v18
	v_exp_f32_e32 v19, v19
	v_pk_fma_f32 v[20:21], v[20:21], v[84:85], v[48:49] op_sel_hi:[1,0,0] neg_lo:[0,0,1] neg_hi:[0,0,1]
	v_exp_f32_e32 v20, v20
	v_exp_f32_e32 v21, v21
	v_pk_fma_f32 v[22:23], v[22:23], v[84:85], v[48:49] op_sel_hi:[1,0,0] neg_lo:[0,0,1] neg_hi:[0,0,1]
	v_exp_f32_e32 v22, v22
	v_exp_f32_e32 v23, v23
	v_pk_fma_f32 v[24:25], v[24:25], v[84:85], v[48:49] op_sel_hi:[1,0,0] neg_lo:[0,0,1] neg_hi:[0,0,1]
	v_exp_f32_e32 v24, v24
	v_exp_f32_e32 v25, v25
	v_pk_fma_f32 v[26:27], v[26:27], v[84:85], v[48:49] op_sel_hi:[1,0,0] neg_lo:[0,0,1] neg_hi:[0,0,1]
	v_exp_f32_e32 v26, v26
	v_exp_f32_e32 v27, v27
	v_pk_fma_f32 v[28:29], v[28:29], v[84:85], v[48:49] op_sel_hi:[1,0,0] neg_lo:[0,0,1] neg_hi:[0,0,1]
	v_exp_f32_e32 v28, v28
	v_exp_f32_e32 v29, v29
	v_pk_fma_f32 v[30:31], v[30:31], v[84:85], v[48:49] op_sel_hi:[1,0,0] neg_lo:[0,0,1] neg_hi:[0,0,1]
	v_exp_f32_e32 v30, v30
	v_exp_f32_e32 v31, v31
	v_pk_fma_f32 v[32:33], v[32:33], v[84:85], v[48:49] op_sel_hi:[1,0,0] neg_lo:[0,0,1] neg_hi:[0,0,1]
	v_exp_f32_e32 v32, v32
	v_exp_f32_e32 v33, v33
	v_pk_add_f32 v[56:57], v[18:19], v[20:21]
	v_pk_add_f32 v[58:59], v[22:23], v[24:25]
	v_pk_add_f32 v[60:61], v[26:27], v[28:29]
	v_pk_add_f32 v[62:63], v[30:31], v[32:33]
	v_pk_add_f32 v[56:57], v[56:57], v[58:59]
	v_pk_add_f32 v[60:61], v[60:61], v[62:63]
	v_pk_add_f32 v[56:57], v[56:57], v[60:61]
	v_add_f32_e32 v50, v56, v57
	v_mov_b32_e32 v51, v50
	s_nop 1
	v_permlane32_swap_b32_e32 v50, v51
	v_add_f32_e32 v50, v50, v51
	v_log_f32_e32 v50, v50
	v_cvt_pk_f16_f32 v40, v18, v19
	v_cvt_pk_f16_f32 v41, v20, v21
	v_cvt_pk_f16_f32 v42, v22, v23
	v_cvt_pk_f16_f32 v43, v24, v25
	v_cvt_pk_f16_f32 v44, v26, v27
	v_cvt_pk_f16_f32 v45, v28, v29
	v_cvt_pk_f16_f32 v46, v30, v31
	v_cvt_pk_f16_f32 v47, v32, v33
	v_add_f32_e32 v50, 0x41600000, v50
	v_mul_f32_e32 v50, 0xbf317218, v50
	v_cndmask_b32_e64 v51, v50, 1.0, vcc
	s_waitcnt vmcnt(0)
	ds_read_b128 v[2:5], v39
	ds_read_b128 v[6:9], v81
	ds_read_b128 v[10:13], v82
	ds_read_b128 v[14:17], v83
	s_waitcnt lgkmcnt(2)
	v_max3_f32 v52, v2, v3, v4
	v_max3_f32 v53, v5, v6, v7
	v_max_f32_e32 v52, v52, v8
	v_max_f32_e32 v53, v53, v9
	s_waitcnt lgkmcnt(0)
	v_max3_f32 v52, v52, v10, v11
	v_max3_f32 v53, v53, v12, v13
	v_max3_f32 v52, v52, v14, v15
	v_max3_f32 v53, v53, v16, v17
	v_max_f32_e32 v52, v52, v53
	v_mov_b32_e32 v53, v52
	s_nop 1
	v_permlane32_swap_b32_e32 v52, v53
	v_max_f32_e32 v52, v52, v53
	v_cndmask_b32_e32 v54, 1.0, v52, vcc
	v_fmamk_f32 v48, v52, 0x3fb8aa3b, v34
	v_pk_fma_f32 v[2:3], v[2:3], v[84:85], v[48:49] op_sel_hi:[1,0,0] neg_lo:[0,0,1] neg_hi:[0,0,1]
	v_mfma_f32_32x32x2_f32 v[64:79], v54, v51, 0
	v_exp_f32_e32 v2, v2
	v_exp_f32_e32 v3, v3
	v_pk_fma_f32 v[4:5], v[4:5], v[84:85], v[48:49] op_sel_hi:[1,0,0] neg_lo:[0,0,1] neg_hi:[0,0,1]
	v_exp_f32_e32 v4, v4
	v_exp_f32_e32 v5, v5
	v_pk_fma_f32 v[6:7], v[6:7], v[84:85], v[48:49] op_sel_hi:[1,0,0] neg_lo:[0,0,1] neg_hi:[0,0,1]
	v_exp_f32_e32 v6, v6
	v_exp_f32_e32 v7, v7
	v_pk_fma_f32 v[8:9], v[8:9], v[84:85], v[48:49] op_sel_hi:[1,0,0] neg_lo:[0,0,1] neg_hi:[0,0,1]
	v_exp_f32_e32 v8, v8
	v_exp_f32_e32 v9, v9
	v_pk_fma_f32 v[10:11], v[10:11], v[84:85], v[48:49] op_sel_hi:[1,0,0] neg_lo:[0,0,1] neg_hi:[0,0,1]
	v_exp_f32_e32 v10, v10
	v_cvt_pk_f16_f32 v56, v2, v3
	v_cvt_pk_f16_f32 v57, v4, v5
	v_cvt_pk_f16_f32 v58, v6, v7
	v_cvt_pk_f16_f32 v59, v8, v9
	v_exp_f32_e32 v11, v11
	v_pk_fma_f32 v[12:13], v[12:13], v[84:85], v[48:49] op_sel_hi:[1,0,0] neg_lo:[0,0,1] neg_hi:[0,0,1]
	v_exp_f32_e32 v12, v12
	v_mfma_f32_32x32x16_f16 v[18:33], v[56:59], v[40:43], 0
	v_exp_f32_e32 v13, v13
	v_pk_fma_f32 v[14:15], v[14:15], v[84:85], v[48:49] op_sel_hi:[1,0,0] neg_lo:[0,0,1] neg_hi:[0,0,1]
	v_exp_f32_e32 v14, v14
	v_exp_f32_e32 v15, v15
	v_pk_fma_f32 v[16:17], v[16:17], v[84:85], v[48:49] op_sel_hi:[1,0,0] neg_lo:[0,0,1] neg_hi:[0,0,1]
	v_exp_f32_e32 v16, v16
	v_exp_f32_e32 v17, v17
	v_cvt_pk_f16_f32 v60, v10, v11
	v_cvt_pk_f16_f32 v61, v12, v13
	v_cvt_pk_f16_f32 v62, v14, v15
	v_cvt_pk_f16_f32 v63, v16, v17
	s_nop 1
	v_mfma_f32_32x32x16_f16 v[18:33], v[60:63], v[44:47], v[18:33]
	s_setprio 3
	s_mov_b32 s40, 0xaaaaaaaa
	s_mov_b32 s41, 0xaaaaaaaa
	s_mov_b32 s42, 0x55555555
	s_mov_b32 s43, 0x55555555
	s_lshl_b32 s25, 2, 16
	s_lshl_b32 s27, 8, 16
	s_lshl_b32 s29, 10, 16
	s_lshl_b32 s31, 16, 16
	s_lshl_b32 s33, 18, 16
	s_lshl_b32 s35, 24, 16
	s_lshl_b32 s37, 26, 16
	v_log_f32_e32 v18, v18
	v_log_f32_e32 v19, v19
	v_log_f32_e32 v20, v20
	v_log_f32_e32 v21, v21
	v_pk_fma_f32 v[64:65], v[18:19], v[84:85], v[64:65] op_sel:[0,1,0] op_sel_hi:[1,1,1]
	v_log_f32_e32 v22, v22
	v_log_f32_e32 v23, v23
	v_pk_fma_f32 v[66:67], v[20:21], v[84:85], v[66:67] op_sel:[0,1,0] op_sel_hi:[1,1,1]
	v_log_f32_e32 v24, v24
	v_log_f32_e32 v25, v25
	s_mov_b64 vcc, s[40:41]
	v_cndmask_b32_dpp v19, v64, v65, vcc quad_perm:[1,0,3,2] row_mask:0xf bank_mask:0xf
	s_mov_b64 vcc, s[42:43]
	v_cndmask_b32_dpp v18, v65, v64, vcc quad_perm:[1,0,3,2] row_mask:0xf bank_mask:0xf
	buffer_store_dwordx2 v[18:19], v36, s[8:11], 0 offen
	v_pk_fma_f32 v[68:69], v[22:23], v[84:85], v[68:69] op_sel:[0,1,0] op_sel_hi:[1,1,1]
	v_log_f32_e32 v26, v26
	v_log_f32_e32 v27, v27
	s_mov_b64 vcc, s[40:41]
	v_cndmask_b32_dpp v21, v66, v67, vcc quad_perm:[1,0,3,2] row_mask:0xf bank_mask:0xf
	s_mov_b64 vcc, s[42:43]
	v_cndmask_b32_dpp v20, v67, v66, vcc quad_perm:[1,0,3,2] row_mask:0xf bank_mask:0xf
	buffer_store_dwordx2 v[20:21], v36, s[8:11], s25 offen
	v_pk_fma_f32 v[70:71], v[24:25], v[84:85], v[70:71] op_sel:[0,1,0] op_sel_hi:[1,1,1]
	v_log_f32_e32 v28, v28
	v_log_f32_e32 v29, v29
	s_mov_b64 vcc, s[40:41]
	v_cndmask_b32_dpp v23, v68, v69, vcc quad_perm:[1,0,3,2] row_mask:0xf bank_mask:0xf
	s_mov_b64 vcc, s[42:43]
	v_cndmask_b32_dpp v22, v69, v68, vcc quad_perm:[1,0,3,2] row_mask:0xf bank_mask:0xf
	buffer_store_dwordx2 v[22:23], v36, s[8:11], s27 offen
	v_pk_fma_f32 v[72:73], v[26:27], v[84:85], v[72:73] op_sel:[0,1,0] op_sel_hi:[1,1,1]
	v_log_f32_e32 v30, v30
	v_log_f32_e32 v31, v31
	s_mov_b64 vcc, s[40:41]
	v_cndmask_b32_dpp v25, v70, v71, vcc quad_perm:[1,0,3,2] row_mask:0xf bank_mask:0xf
	s_mov_b64 vcc, s[42:43]
	v_cndmask_b32_dpp v24, v71, v70, vcc quad_perm:[1,0,3,2] row_mask:0xf bank_mask:0xf
	buffer_store_dwordx2 v[24:25], v36, s[8:11], s29 offen
	v_pk_fma_f32 v[74:75], v[28:29], v[84:85], v[74:75] op_sel:[0,1,0] op_sel_hi:[1,1,1]
	v_log_f32_e32 v32, v32
	v_log_f32_e32 v33, v33
	s_mov_b64 vcc, s[40:41]
	v_cndmask_b32_dpp v27, v72, v73, vcc quad_perm:[1,0,3,2] row_mask:0xf bank_mask:0xf
	s_mov_b64 vcc, s[42:43]
	v_cndmask_b32_dpp v26, v73, v72, vcc quad_perm:[1,0,3,2] row_mask:0xf bank_mask:0xf
	buffer_store_dwordx2 v[26:27], v36, s[8:11], s31 offen
	v_pk_fma_f32 v[76:77], v[30:31], v[84:85], v[76:77] op_sel:[0,1,0] op_sel_hi:[1,1,1]
	s_mov_b64 vcc, s[40:41]
	v_cndmask_b32_dpp v29, v74, v75, vcc quad_perm:[1,0,3,2] row_mask:0xf bank_mask:0xf
	s_mov_b64 vcc, s[42:43]
	v_cndmask_b32_dpp v28, v75, v74, vcc quad_perm:[1,0,3,2] row_mask:0xf bank_mask:0xf
	buffer_store_dwordx2 v[28:29], v36, s[8:11], s33 offen
	v_pk_fma_f32 v[78:79], v[32:33], v[84:85], v[78:79] op_sel:[0,1,0] op_sel_hi:[1,1,1]
	s_mov_b64 vcc, s[40:41]
	v_cndmask_b32_dpp v31, v76, v77, vcc quad_perm:[1,0,3,2] row_mask:0xf bank_mask:0xf
	s_mov_b64 vcc, s[42:43]
	v_cndmask_b32_dpp v30, v77, v76, vcc quad_perm:[1,0,3,2] row_mask:0xf bank_mask:0xf
	buffer_store_dwordx2 v[30:31], v36, s[8:11], s35 offen
	s_nop 0
	s_mov_b64 vcc, s[40:41]
	v_cndmask_b32_dpp v33, v78, v79, vcc quad_perm:[1,0,3,2] row_mask:0xf bank_mask:0xf
	s_mov_b64 vcc, s[42:43]
	v_cndmask_b32_dpp v32, v79, v78, vcc quad_perm:[1,0,3,2] row_mask:0xf bank_mask:0xf
	buffer_store_dwordx2 v[32:33], v36, s[8:11], s37 offen
	s_endpgm
